# expert gate/up K-loop moved by 40 bytes (instruction placement), on top of nt weight stores in the conversion phase
# speedup vs baseline: 1.0161x; 1.0038x over previous
; template <class Epi, class Sched>
; __device__ __forceinline__ void gemm_phase(LAS unsigned char* lds, const int K, const Sched& S, const Epi& E) {
;     ...
;         const bool has_next = S.next(ui + 1, nxt);
;         const char* nA = has_next ? nxt.A : cA; const char* nB = has_next ? nxt.B : cB;
; #pragma unroll 1
;         for (int t = 0; t < nt; t += 2) {
;             const bool last = (t == nt - 2);
;             const char* a1 = cA + (size_t)(t + 1) * kstep;
;             const char* a2 = last ? nA : cA + (size_t)(t + 2) * kstep; const char* b2 = last ? nB : cB + (size_t)(t + 2) * kstep;
;             const char* a3 = a2 + kstep; const char* b3 = b2 + kstep;
;     __device__ __forceinline__ void init(f32x4 (&acc)[2][2][4][2], const g8::Unit&, int, int) const {
; #pragma unroll
;         for (int a = 0; a < 2; ++a)
; #pragma unroll
;             for (int b = 0; b < 2; ++b)
; #pragma unroll
;                 for (int m = 0; m < 4; ++m)
; #pragma unroll
;                     for (int n = 0; n < 2; ++n) acc[a][b][m][n] = (f32x4){0.f, 0.f, 0.f, 0.f}; }
.LBB0_2524:
	s_lshl_b32 s22, s53, 10
	s_add_i32 s22, s22, 0
	s_add_i32 s22, s22, 0x20000
	v_add3_u32 v201, s22, v194, v195
	v_add3_u32 v215, s22, v196, v197
	s_add_u32 s22, s0, 0x80
	s_addc_u32 s23, s1, 0
	s_add_u32 s55, s24, 0x100
	v_mov_b32_e32 v2, 0
	s_addc_u32 s56, s25, 0
	s_mov_b32 s57, -2
	v_mov_b32_e32 v3, v2
	v_mov_b32_e32 v4, v2
	v_mov_b32_e32 v5, v2
	v_mov_b32_e32 v6, v2
	v_mov_b32_e32 v7, v2
	v_mov_b32_e32 v8, v2
	v_mov_b32_e32 v9, v2
	v_mov_b32_e32 v18, v2
	v_mov_b32_e32 v19, v2
	v_mov_b32_e32 v20, v2
	v_mov_b32_e32 v21, v2
	v_mov_b32_e32 v22, v2
	v_mov_b32_e32 v23, v2
	v_mov_b32_e32 v24, v2
	v_mov_b32_e32 v25, v2
	v_mov_b32_e32 v34, v2
	v_mov_b32_e32 v35, v2
	v_mov_b32_e32 v36, v2
	v_mov_b32_e32 v37, v2
	v_mov_b32_e32 v38, v2
	v_mov_b32_e32 v39, v2
	v_mov_b32_e32 v40, v2
	v_mov_b32_e32 v41, v2
	v_mov_b32_e32 v50, v2
	v_mov_b32_e32 v51, v2
	v_mov_b32_e32 v52, v2
	v_mov_b32_e32 v53, v2
	v_mov_b32_e32 v54, v2
	v_mov_b32_e32 v55, v2
	v_mov_b32_e32 v56, v2
	v_mov_b32_e32 v57, v2
	v_mov_b32_e32 v10, v2
	v_mov_b32_e32 v11, v2
	v_mov_b32_e32 v12, v2
	v_mov_b32_e32 v13, v2
	v_mov_b32_e32 v14, v2
	v_mov_b32_e32 v15, v2
	v_mov_b32_e32 v16, v2
	v_mov_b32_e32 v17, v2
	v_mov_b32_e32 v26, v2
	v_mov_b32_e32 v27, v2
	v_mov_b32_e32 v28, v2
	v_mov_b32_e32 v29, v2
	v_mov_b32_e32 v30, v2
	v_mov_b32_e32 v31, v2
	v_mov_b32_e32 v32, v2
	v_mov_b32_e32 v33, v2
	v_mov_b32_e32 v42, v2
	v_mov_b32_e32 v43, v2
	v_mov_b32_e32 v44, v2
	v_mov_b32_e32 v45, v2
	v_mov_b32_e32 v46, v2
	v_mov_b32_e32 v47, v2
	v_mov_b32_e32 v48, v2
	v_mov_b32_e32 v49, v2
	v_mov_b32_e32 v58, v2
	v_mov_b32_e32 v59, v2
	v_mov_b32_e32 v60, v2
	v_mov_b32_e32 v61, v2
	v_mov_b32_e32 v62, v2
	v_mov_b32_e32 v63, v2
	v_mov_b32_e32 v64, v2
	v_mov_b32_e32 v65, v2
	v_mov_b32_e32 v66, v2
	v_mov_b32_e32 v67, v2
	v_mov_b32_e32 v68, v2
	v_mov_b32_e32 v69, v2
	v_mov_b32_e32 v70, v2
	v_mov_b32_e32 v71, v2
	v_mov_b32_e32 v72, v2
	v_mov_b32_e32 v73, v2
	v_mov_b32_e32 v82, v2
	v_mov_b32_e32 v83, v2
	v_mov_b32_e32 v84, v2
	v_mov_b32_e32 v85, v2
	v_mov_b32_e32 v86, v2
	v_mov_b32_e32 v87, v2
	v_mov_b32_e32 v88, v2
	v_mov_b32_e32 v89, v2
	v_mov_b32_e32 v98, v2
	v_mov_b32_e32 v99, v2
	v_mov_b32_e32 v100, v2
	v_mov_b32_e32 v101, v2
	v_mov_b32_e32 v102, v2
	v_mov_b32_e32 v103, v2
	v_mov_b32_e32 v104, v2
	v_mov_b32_e32 v105, v2
	v_mov_b32_e32 v114, v2
	v_mov_b32_e32 v115, v2
	v_mov_b32_e32 v116, v2
	v_mov_b32_e32 v117, v2
	v_mov_b32_e32 v118, v2
	v_mov_b32_e32 v119, v2
	v_mov_b32_e32 v120, v2
	v_mov_b32_e32 v121, v2
	v_mov_b32_e32 v74, v2
	v_mov_b32_e32 v75, v2
	v_mov_b32_e32 v76, v2
	v_mov_b32_e32 v77, v2
	v_mov_b32_e32 v78, v2
	v_mov_b32_e32 v79, v2
	v_mov_b32_e32 v80, v2
	v_mov_b32_e32 v81, v2
	v_mov_b32_e32 v90, v2
	v_mov_b32_e32 v91, v2
	v_mov_b32_e32 v92, v2
	v_mov_b32_e32 v93, v2
	v_mov_b32_e32 v94, v2
	v_mov_b32_e32 v95, v2
	v_mov_b32_e32 v96, v2
	v_mov_b32_e32 v97, v2
	v_mov_b32_e32 v106, v2
	v_mov_b32_e32 v107, v2
	v_mov_b32_e32 v108, v2
	v_mov_b32_e32 v109, v2
	v_mov_b32_e32 v110, v2
	v_mov_b32_e32 v111, v2
	v_mov_b32_e32 v112, v2
	v_mov_b32_e32 v113, v2
	v_mov_b32_e32 v122, v2
	v_mov_b32_e32 v123, v2
	v_mov_b32_e32 v124, v2
	v_mov_b32_e32 v125, v2
	v_mov_b32_e32 v126, v2
	v_mov_b32_e32 v127, v2
	v_mov_b32_e32 v128, v2
	v_mov_b32_e32 v129, v2
	s_branch .LBB0_2527
	s_nop 0
	s_nop 0
	s_nop 0
	s_nop 0
	s_nop 0
	s_nop 0
	s_nop 0
	s_nop 0
	s_nop 0
	s_nop 0

; #define G8_STAGE(bufoff, gbase, voff) do { _Pragma("unroll") for (int _i = 0; _i < 2; ++_i) \
;         __builtin_amdgcn_global_load_lds((const unsigned*)((const char*)(gbase) + (voff)[_i]), (LAS unsigned*)(lds + (bufoff) + ldsw + _i * 8192), 16, 0, 0); } while (0)
; #define G8_LDA(dst, b, h) do { _Pragma("unroll") for (int m = 0; m < 4; ++m) _Pragma("unroll") for (int k = 0; k < 2; ++k) dst[m][k] = *(const LAS bf16x8*)(lds + G8_SA(b, h) + aoff + m * 2048 + k * 1024); } while (0)
; #define G8_LDB(dst, b, h) do { _Pragma("unroll") for (int n = 0; n < 2; ++n) _Pragma("unroll") for (int k = 0; k < 2; ++k) dst[n][k] = *(const LAS bf16x8*)(lds + G8_SB(b, h) + boff + n * 2048 + k * 1024); } while (0)
; #define G8_SCHED __builtin_amdgcn_sched_barrier(0)
; template <class Epi, class Sched>
; __device__ __forceinline__ void gemm_phase(LAS unsigned char* lds, const int K, const Sched& S, const Epi& E) {
;     ...
;             const bool last = (t == nt - 2);
;             const char* a1 = cA + (size_t)(t + 1) * kstep;
;             const char* a2 = last ? nA : cA + (size_t)(t + 2) * kstep; const char* b2 = last ? nB : cB + (size_t)(t + 2) * kstep;
;             const char* a3 = a2 + kstep; const char* b3 = b2 + kstep;
;             G8_LDB(B0, 0, 0); G8_SCHED; G8_LDA(At, 0, 0); G8_STAGE(G8_SA(1, 1), a1, oc[1]);
;             if (last && has_next) S.aoff(nxt, tid, oc);
.LBB0_2527:
	v_add_u32_e32 v130, 0, v198
	v_add_u32_e32 v142, 0x10000, v130
	ds_read_b128 v[130:133], v142
	ds_read_b128 v[134:137], v142 offset:1024
	ds_read_b128 v[138:141], v142 offset:2048
	ds_read_b128 v[142:145], v142 offset:3072
	s_cmp_eq_u32 s57, 12
	s_cselect_b64 s[24:25], -1, 0
	s_add_i32 m0, s42, 0xc000
	ds_read_b128 v[170:173], v200
	ds_read_b128 v[174:177], v200 offset:1024
	ds_read_b128 v[162:165], v200 offset:2048
	ds_read_b128 v[166:169], v200 offset:3072
	ds_read_b128 v[154:157], v200 offset:4096
	ds_read_b128 v[158:161], v200 offset:5120
	ds_read_b128 v[146:149], v200 offset:6144
	ds_read_b128 v[150:153], v200 offset:7168
	global_load_lds_dwordx4 v184, s[22:23]
	s_add_i32 m0, s42, 0xe000
	s_and_b64 s[34:35], s[10:11], s[24:25]
	global_load_lds_dwordx4 v186, s[22:23]
	s_andn2_b64 vcc, exec, s[34:35]
	s_cbranch_vccz .LBB0_2525
	v_mov_b32_e32 v185, v1
	v_mov_b32_e32 v187, v1
	v_mov_b64_e32 v[190:191], v[184:185]
	s_branch .LBB0_2526
	s_nop 0
	s_nop 0
	s_nop 0
	s_nop 0
	s_nop 0
	s_nop 0
